# speedup vs baseline: 1.0036x; 1.0036x over previous
.LBB2_13:
	s_waitcnt vmcnt(0)
	s_barrier
	v_add_u32_e32 v34, s22, v109
	v_add_u32_e32 v34, 0xffff4000, v34
	v_and_b32_e32 v34, 0xc000, v34
	v_add_u32_e32 v114, 0, v34
	v_add_u32_e32 v38, v114, v106
	v_add_u32_e32 v82, v114, v105
	ds_read_b128 v[34:37], v38
	ds_read_b128 v[38:41], v38 offset:4096
	ds_read_b128 v[116:119], v82
	ds_read_b128 v[120:123], v82 offset:4096
	v_add_u32_e32 v82, v114, v104
	s_waitcnt lgkmcnt(2)
	v_mfma_f32_32x32x16_f16 v[50:65], v[34:37], v[78:81], 0
	v_mfma_f32_32x32x16_f16 v[34:49], v[38:41], v[78:81], 0
	s_waitcnt lgkmcnt(1)
	v_mfma_f32_32x32x16_f16 v[50:65], v[116:119], v[74:77], v[50:65]
	s_waitcnt lgkmcnt(0)
	v_mfma_f32_32x32x16_f16 v[34:49], v[120:123], v[74:77], v[34:49]
	ds_read_b128 v[116:119], v82
	ds_read_b128 v[120:123], v82 offset:4096
	v_add_u32_e32 v82, v114, v103
	s_add_i32 s16, s22, 0xffffc000
	s_and_b32 s16, s16, 0xc000
	v_add_u32_e32 v124, s16, v108
	s_add_u32 s16, s12, 0xfffce000
	s_addc_u32 s17, s13, -1
	v_readfirstlane_b32 s26, v124
	v_lshl_add_u64 v[124:125], s[16:17], 0, v[84:85]
	s_mov_b32 s27, m0
	s_mov_b32 m0, s26
	s_nop 0
	global_load_lds_dwordx4 v[124:125], off
	s_mov_b32 m0, s27
	v_lshl_add_u64 v[124:125], s[16:17], 0, v[86:87]
	s_add_i32 s16, s26, 0x400
	s_mov_b32 s17, m0
	s_mov_b32 m0, s16
	s_nop 0
	global_load_lds_dwordx4 v[124:125], off
	s_mov_b32 m0, s17
	s_and_b32 s16, s22, 0xc000
	v_add_u32_e32 v124, s16, v108
	s_nop 0
	v_readfirstlane_b32 s16, v124
	v_lshl_add_u64 v[124:125], s[12:13], 0, v[84:85]
	s_mov_b32 s17, m0
	s_mov_b32 m0, s16
	s_nop 0
	global_load_lds_dwordx4 v[124:125], off
	s_mov_b32 m0, s17
	v_lshl_add_u64 v[124:125], s[12:13], 0, v[86:87]
	s_addk_i32 s16, 0x400
	s_mov_b32 s17, m0
	s_mov_b32 m0, s16
	s_nop 0
	global_load_lds_dwordx4 v[124:125], off
	s_mov_b32 m0, s17
	s_waitcnt lgkmcnt(1)
	v_mfma_f32_32x32x16_f16 v[50:65], v[116:119], v[70:73], v[50:65]
	s_waitcnt lgkmcnt(0)
	v_mfma_f32_32x32x16_f16 v[34:49], v[120:123], v[70:73], v[34:49]
	ds_read_b128 v[116:119], v82
	ds_read_b128 v[120:123], v82 offset:4096
	s_waitcnt lgkmcnt(1)
	v_mfma_f32_32x32x16_f16 v[50:65], v[116:119], v[66:69], v[50:65]
	s_waitcnt lgkmcnt(0)
	v_mfma_f32_32x32x16_f16 v[34:49], v[120:123], v[66:69], v[34:49]
	s_nop 9
	v_max3_f32 v82, v50, v51, v52
	v_max3_f32 v82, v82, v53, v54
	v_max3_f32 v82, v82, v55, v56
	v_max3_f32 v82, v82, v57, v58
	v_max3_f32 v82, v82, v59, v60
	v_max3_f32 v82, v82, v61, v62
	v_max_f32_e32 v91, v65, v65
	v_max3_f32 v89, v34, v35, v36
	v_max3_f32 v89, v89, v37, v38
	v_max3_f32 v89, v89, v39, v40
	v_max3_f32 v89, v89, v41, v42
	v_max3_f32 v89, v89, v43, v44
	v_max3_f32 v89, v89, v45, v46
	v_max_f32_e32 v90, v49, v49
	v_max3_f32 v82, v82, v63, v64
	v_max3_f32 v89, v89, v47, v48
	v_max_f32_e32 v90, v91, v90
	v_max3_f32 v82, v82, v89, v90
	v_mov_b32_e32 v89, v82
	s_nop 1
	v_permlane32_swap_b32_e32 v82, v89
	v_max_f32_e32 v82, v82, v89
	v_fma_f32 v89, v82, s23, -v88
	v_cmp_lt_f32_e32 vcc, s24, v89
	s_cbranch_vccz .LBB2_16
	v_mul_f32_e32 v82, 0x3e38aa3b, v82
	v_max_f32_e32 v82, v82, v82
	v_max_f32_e32 v89, v88, v88
	v_max_f32_e32 v102, v89, v82
	v_sub_f32_e32 v82, v88, v102
	v_exp_f32_e32 v82, v82
	s_and_saveexec_b64 s[16:17], s[4:5]
	s_cbranch_execz .LBB2_11
	v_lshl_add_u32 v88, v95, 2, v100
	ds_write_b32 v88, v82
	s_branch .LBB2_11
